# v82 + T-phase gate reuse/hoist + thin1 three-rows-ahead prefetch (three landing register sets)
# speedup vs baseline: 1.0030x; 1.0030x over previous
.LBB0_267:
	v_readlane_b32 s18, v252, 1
	v_readlane_b32 s2, v254, 39
	v_readlane_b32 s19, v252, 2
	s_waitcnt lgkmcnt(0)
	v_mov_b32_e32 v4, s2
	v_readlane_b32 s2, v254, 40
	s_barrier
	v_mbcnt_lo_u32_b32 v26, -1, 0
	v_mbcnt_hi_u32_b32 v26, -1, v26
	v_readlane_b32 s6, v252, 6
	v_mov_b32_e32 v5, s2
	ds_read_b32 v0, v4
	ds_read_b32 v1, v5
	v_readlane_b32 s2, v252, 7
	s_add_i32 s36, s6, s2
	s_lshl_b32 s96, s72, 6
	s_waitcnt lgkmcnt(1)
	v_readfirstlane_b32 s2, v0
	s_waitcnt lgkmcnt(0)
	v_readfirstlane_b32 s3, v1
	s_lshl_b64 s[54:55], s[96:97], 2
	v_lshlrev_b32_e32 v0, 2, v26
	s_add_u32 s2, s2, s54
	v_and_b32_e32 v16, 28, v0
	s_addc_u32 s3, s3, s55
	v_lshlrev_b32_e32 v160, 2, v16
	global_load_dwordx4 v[0:3], v160, s[2:3]
	ds_read_b32 v4, v4
	ds_read_b32 v5, v5
	v_ashrrev_i32_e32 v27, 31, v26
	v_lshlrev_b32_e32 v68, 3, v26
	s_waitcnt lgkmcnt(1)
	v_readfirstlane_b32 s2, v4
	s_waitcnt lgkmcnt(0)
	v_readfirstlane_b32 s3, v5
	s_add_u32 s2, s2, s54
	s_addc_u32 s3, s3, s55
	s_nop 2
	global_load_dwordx4 v[4:7], v160, s[2:3] offset:128
	v_readlane_b32 s2, v254, 41
	s_nop 1
	v_mov_b32_e32 v8, s2
	v_readlane_b32 s2, v254, 42
	ds_read_b32 v8, v8
	s_nop 0
	v_mov_b32_e32 v9, s2
	ds_read_b32 v10, v9
	v_and_b32_e32 v9, 31, v26
	s_waitcnt lgkmcnt(1)
	v_readfirstlane_b32 s2, v8
	v_lshlrev_b32_e32 v8, 3, v9
	s_waitcnt lgkmcnt(0)
	v_readfirstlane_b32 s3, v10
	s_add_u32 s2, s2, s54
	s_addc_u32 s3, s3, s55
	s_lshl_b32 s96, s72, 7
	s_nop 1
	global_load_dwordx2 v[28:29], v8, s[2:3]
	v_readlane_b32 s2, v254, 43
	s_lshl_b64 s[4:5], s[96:97], 2
	s_nop 0
	v_mov_b32_e32 v10, s2
	v_readlane_b32 s2, v254, 44
	ds_read_b32 v10, v10
	s_nop 0
	v_mov_b32_e32 v11, s2
	ds_read_b32 v11, v11
	s_waitcnt lgkmcnt(1)
	v_readfirstlane_b32 s2, v10
	s_waitcnt lgkmcnt(0)
	v_readfirstlane_b32 s3, v11
	s_add_u32 s2, s2, s4
	v_writelane_b32 v255, s4, 42
	s_addc_u32 s3, s3, s5
	v_lshlrev_b64 v[10:11], 3, v[26:27]
	v_lshl_add_u64 v[12:13], s[2:3], 0, v[10:11]
	v_readlane_b32 s2, v254, 45
	global_load_dwordx2 v[24:25], v[12:13], off
	s_lshl_b32 s96, s72, 8
	v_mov_b32_e32 v14, s2
	v_readlane_b32 s2, v254, 46
	ds_read_b32 v12, v14
	s_lshl_b64 s[50:51], s[96:97], 2
	v_mov_b32_e32 v15, s2
	ds_read_b32 v13, v15
	v_writelane_b32 v255, s5, 43
	s_waitcnt lgkmcnt(1)
	v_readfirstlane_b32 s2, v12
	s_waitcnt lgkmcnt(0)
	v_readfirstlane_b32 s3, v13
	s_add_u32 s2, s2, s50
	s_addc_u32 s3, s3, s51
	v_lshl_add_u64 v[12:13], s[2:3], 0, v[10:11]
	global_load_dwordx2 v[30:31], v[12:13], off
	ds_read_b32 v12, v14
	ds_read_b32 v13, v15
	s_waitcnt lgkmcnt(1)
	v_readfirstlane_b32 s2, v12
	s_waitcnt lgkmcnt(0)
	v_readfirstlane_b32 s3, v13
	s_add_u32 s2, s2, s50
	s_addc_u32 s3, s3, s51
	v_lshl_add_u64 v[10:11], s[2:3], 0, v[10:11]
	global_load_dwordx2 v[32:33], v[10:11], off offset:512
	v_readlane_b32 s2, v254, 47
	s_cmpk_gt_i32 s36, 0x7fff
	s_nop 0
	v_mov_b32_e32 v10, s2
	v_readlane_b32 s2, v254, 48
	ds_read_b32 v10, v10
	s_nop 0
	v_mov_b32_e32 v11, s2
	ds_read_b32 v11, v11
	s_waitcnt lgkmcnt(1)
	v_readfirstlane_b32 s2, v10
	s_waitcnt lgkmcnt(0)
	v_readfirstlane_b32 s3, v11
	s_cbranch_scc1 .LBB0_272
	s_add_u32 s22, s18, 0x100000
	s_addc_u32 s23, s19, 0
	s_add_u32 s38, s18, 0x140000
	s_addc_u32 s39, s19, 0
	s_lshl_b32 s7, s36, 4
	s_lshr_b32 s31, s36, 2
	s_and_b32 s10, s7, 0x3f0
	s_and_b32 s31, s31, 0x1f0
	s_or_b32 s11, s10, 0x70800
	s_or_b32 s33, s31, 0x70200
	v_cmp_lt_u32_e64 s[40:41], 15, v9
	v_mov_b32_e32 v10, s33
	v_mov_b32_e32 v11, s11
	v_cndmask_b32_e64 v10, v10, v11, s[40:41]
	v_lshlrev_b32_e32 v10, 2, v10
	v_mov_b32_e32 v11, v161
	v_and_b32_e32 v8, 56, v8
	v_mov_b32_e32 v9, v161
	v_lshl_add_u64 v[10:11], s[22:23], 0, v[10:11]
	v_lshl_add_u64 v[10:11], v[10:11], 0, v[8:9]
	s_or_b32 s11, s31, 0x70000
	global_load_dwordx2 v[50:51], v[10:11], off
	s_or_b32 s10, s10, 0x70400
	v_mov_b32_e32 v10, s11
	s_lshl_b32 s11, s36, 7
	v_mov_b32_e32 v11, s10
	s_lshl_b32 s10, s36, 5
	s_and_b32 s11, s11, 0x3ff80
	v_lshl_add_u64 v[36:37], s[38:39], 0, v[160:161]
	v_cndmask_b32_e64 v10, v10, v11, s[40:41]
	s_add_u32 s38, s38, s11
	v_lshlrev_b32_e32 v10, 2, v10
	v_mov_b32_e32 v11, v161
	s_addc_u32 s39, s39, 0
	v_lshl_add_u64 v[34:35], s[22:23], 0, v[160:161]
	v_lshl_add_u64 v[38:39], s[22:23], 0, v[8:9]
	v_lshl_add_u64 v[10:11], s[22:23], 0, v[10:11]
	s_add_u32 s22, s22, s11
	v_lshl_add_u64 v[8:9], v[10:11], 0, v[8:9]
	s_addc_u32 s23, s23, 0
	s_ashr_i32 s37, s36, 31
	s_mul_i32 s31, s36, 0x1a00
	global_load_dwordx2 v[44:45], v[8:9], off
	global_load_dwordx4 v[12:15], v160, s[22:23]
	s_mul_hi_i32 s11, s36, 0x1a00
	global_load_dwordx4 v[8:11], v160, s[38:39]
	s_add_u32 s22, s18, s31
	s_addc_u32 s23, s19, s11
	s_add_u32 s22, s22, 0x6400000
	s_addc_u32 s23, s23, 0
	v_lshlrev_b64 v[20:21], 2, v[26:27]
	v_and_b32_e32 v18, 0xffffffc0, v68
	v_lshl_add_u64 v[22:23], s[22:23], 0, v[20:21]
	s_movk_i32 s33, 0x1000
	v_ashrrev_i32_e32 v19, 31, v18
	v_add_co_u32_e32 v40, vcc, s33, v22
	v_lshlrev_b64 v[18:19], 1, v[18:19]
	s_nop 0
	v_addc_co_u32_e32 v41, vcc, 0, v23, vcc
	v_readlane_b32 s12, v255, 42
	global_load_dword v76, v[40:41], off offset:1024
	global_load_dword v69, v[22:23], off offset:3584
	global_load_dword v70, v[22:23], off offset:3328
	global_load_dword v73, v[22:23], off offset:3072
	v_lshl_add_u64 v[22:23], s[22:23], 0, v[18:19]
	v_lshlrev_b32_e32 v160, 1, v16
	v_readlane_b32 s13, v255, 43
	s_add_u32 s2, s2, s12
	v_lshl_add_u64 v[16:17], v[22:23], 0, v[160:161]
	s_addc_u32 s3, s3, s13
	global_load_dwordx2 v[60:61], v[16:17], off offset:1088
	global_load_dwordx2 v[62:63], v[16:17], off offset:1024
	v_lshl_add_u64 v[16:17], v[26:27], 3, s[2:3]
	global_load_dwordx2 v[40:41], v[16:17], off
	v_and_b32_e32 v16, 8, v26
	v_cmp_eq_u32_e64 s[42:43], 0, v16
	v_and_b32_e32 v16, 7, v26
	v_lshl_or_b32 v16, v16, 3, s31
	v_mov_b32_e32 v17, s11
	s_lshl_b64 s[2:3], s[36:37], 10
	v_lshl_add_u64 v[46:47], v[16:17], 0, v[18:19]
	v_mov_b32_e32 v16, 0x1a00
	v_lshl_add_u64 v[42:43], s[2:3], 0, v[20:21]
	v_mad_i64_i32 v[48:49], s[2:3], s36, v16, v[20:21]
	s_mov_b64 s[4:5], 0x200000
	s_mov_b32 s11, s36
	s_waitcnt vmcnt(10)
	v_mov_b64_e32 v[54:55], v[50:51]
	s_waitcnt vmcnt(9)
	v_mov_b64_e32 v[52:53], v[44:45]
	s_waitcnt vmcnt(8)
	v_mov_b64_e32 v[18:19], v[14:15]
	v_mov_b64_e32 v[16:17], v[12:13]
	s_waitcnt vmcnt(7)
	v_mov_b64_e32 v[22:23], v[10:11]
	v_mov_b64_e32 v[20:21], v[8:9]
	s_waitcnt vmcnt(6)
	v_mov_b32_e32 v75, v76
	s_waitcnt vmcnt(5)
	v_mov_b32_e32 v74, v69
	s_waitcnt vmcnt(4)
	v_mov_b32_e32 v72, v70
	s_waitcnt vmcnt(3)
	v_mov_b32_e32 v71, v73
	s_waitcnt vmcnt(2)
	v_mov_b64_e32 v[56:57], v[60:61]
	s_waitcnt vmcnt(1)
	v_mov_b64_e32 v[58:59], v[62:63]
	s_waitcnt vmcnt(0)
	v_lshl_add_u64 v[66:67], s[18:19], 0, v[46:47]
	v_lshl_add_u64 v[64:65], s[18:19], 0, v[48:49]
	s_and_b32 s22, s10, 0xffe0
	s_lshr_b32 s31, s11, 2
	v_add_co_u32_e32 v96, vcc, 0x7100000, v66
	s_lshl_b32 s96, s22, 2
	s_and_b32 s22, s7, 0x3f0
	s_and_b32 s31, s31, 0x1f0
	v_addc_co_u32_e32 v97, vcc, 0, v67, vcc
	s_or_b32 s23, s22, 0x70400
	s_or_b32 s33, s31, 0x70000
	v_add_co_u32_e32 v98, vcc, 0x7100000, v64
	v_mov_b32_e32 v102, s33
	v_mov_b32_e32 v103, s23
	s_or_b32 s22, s22, 0x70800
	s_or_b32 s23, s31, 0x70200
	v_addc_co_u32_e32 v99, vcc, 0, v65, vcc
	v_cndmask_b32_e64 v102, v102, v103, s[40:41]
	v_mov_b32_e32 v106, s23
	v_mov_b32_e32 v107, s22
	global_load_dwordx2 v[110:111], v[96:97], off offset:1024
	global_load_dwordx2 v[108:109], v[96:97], off offset:1088
	global_load_dword v112, v[98:99], off offset:3072
	global_load_dword v113, v[98:99], off offset:3328
	v_add_co_u32_e32 v96, vcc, 0x7101000, v64
	v_lshlrev_b32_e32 v160, 2, v102
	v_cndmask_b32_e64 v106, v106, v107, s[40:41]
	v_addc_co_u32_e32 v97, vcc, 0, v65, vcc
	v_lshl_add_u64 v[100:101], v[34:35], 0, s[96:97]
	v_lshl_add_u64 v[104:105], v[38:39], 0, v[160:161]
	v_lshlrev_b32_e32 v160, 2, v106
	global_load_dword v114, v[98:99], off offset:3584
	global_load_dword v115, v[96:97], off offset:1024
	s_nop 0
	global_load_dwordx4 v[96:99], v[100:101], off
	v_lshl_add_u64 v[100:101], v[36:37], 0, s[96:97]
	v_lshl_add_u64 v[106:107], v[38:39], 0, v[160:161]
	global_load_dwordx4 v[100:103], v[100:101], off
	s_nop 0
	global_load_dwordx2 v[104:105], v[104:105], off
	s_nop 0
	global_load_dwordx2 v[106:107], v[106:107], off
	s_and_b32 s22, s10, 0xffe0
	s_lshr_b32 s31, s11, 2
	v_add_co_u32_e32 v116, vcc, 0x7e00000, v66
	s_lshl_b32 s96, s22, 2
	s_and_b32 s22, s7, 0x3f0
	s_and_b32 s31, s31, 0x1f0
	v_addc_co_u32_e32 v117, vcc, 0, v67, vcc
	s_or_b32 s23, s22, 0x70400
	s_or_b32 s33, s31, 0x70000
	v_add_co_u32_e32 v118, vcc, 0x7e00000, v64
	v_mov_b32_e32 v122, s33
	v_mov_b32_e32 v123, s23
	s_or_b32 s22, s22, 0x70800
	s_or_b32 s23, s31, 0x70200
	v_addc_co_u32_e32 v119, vcc, 0, v65, vcc
	v_cndmask_b32_e64 v122, v122, v123, s[40:41]
	v_mov_b32_e32 v126, s23
	v_mov_b32_e32 v127, s22
	global_load_dwordx2 v[130:131], v[116:117], off offset:1024
	global_load_dwordx2 v[128:129], v[116:117], off offset:1088
	global_load_dword v132, v[118:119], off offset:3072
	global_load_dword v133, v[118:119], off offset:3328
	v_add_co_u32_e32 v116, vcc, 0x7e01000, v64
	v_lshlrev_b32_e32 v160, 2, v122
	v_cndmask_b32_e64 v126, v126, v127, s[40:41]
	v_addc_co_u32_e32 v117, vcc, 0, v65, vcc
	v_lshl_add_u64 v[120:121], v[34:35], 0, s[96:97]
	v_lshl_add_u64 v[124:125], v[38:39], 0, v[160:161]
	v_lshlrev_b32_e32 v160, 2, v126
	global_load_dword v134, v[118:119], off offset:3584
	global_load_dword v135, v[116:117], off offset:1024
	s_nop 0
	global_load_dwordx4 v[116:119], v[120:121], off
	v_lshl_add_u64 v[120:121], v[36:37], 0, s[96:97]
	v_lshl_add_u64 v[126:127], v[38:39], 0, v[160:161]
	global_load_dwordx4 v[120:123], v[120:121], off
	s_nop 0
	global_load_dwordx2 v[124:125], v[124:125], off
	s_nop 0
	global_load_dwordx2 v[126:127], v[126:127], off
	s_mov_b32 s99, 0
	s_branch .LBB0_270
.LBB0_269:
	v_lshlrev_b32_e32 v78, 16, v63
	v_and_b32_e32 v79, 0xffff0000, v63
	v_lshlrev_b32_e32 v84, 16, v62
	v_and_b32_e32 v85, 0xffff0000, v62
	v_lshlrev_b32_e32 v62, 16, v60
	v_and_b32_e32 v63, 0xffff0000, v60
	v_lshlrev_b32_e32 v80, 16, v61
	v_and_b32_e32 v81, 0xffff0000, v61
	v_pk_mul_f32 v[60:61], v[62:63], v[62:63]
	v_pk_mul_f32 v[82:83], v[80:81], v[80:81]
	v_pk_fma_f32 v[60:61], v[84:85], v[84:85], v[60:61]
	v_pk_fma_f32 v[82:83], v[78:79], v[78:79], v[82:83]
	v_add_f32_e32 v60, v60, v61
	v_add_f32_e32 v60, v60, v82
	v_add_f32_e32 v60, v60, v83
	s_mov_b32 s22, 0x6400000
	s_addk_i32 s11, 0x800
	v_add_f32_dpp v60, v60, v60 quad_perm:[1,0,3,2] row_mask:0xf bank_mask:0xf bound_ctrl:1
	s_add_i32 s10, s10, 0x10000
	s_add_i32 s7, s7, 0x8000
	v_add_f32_dpp v60, v60, v60 quad_perm:[2,3,0,1] row_mask:0xf bank_mask:0xf bound_ctrl:1
	s_nop 1
	v_add_f32_dpp v60, v60, v60 row_half_mirror row_mask:0xf bank_mask:0xf bound_ctrl:1
	v_fmamk_f32 v60, v60, 0x3c800000, v240
	v_rsq_f32_e32 v60, v60
	s_nop 0
	v_pk_mul_f32 v[62:63], v[60:61], v[62:63] op_sel_hi:[0,1]
	v_pk_mul_f32 v[82:83], v[60:61], v[84:85] op_sel_hi:[0,1]
	v_pk_mul_f32 v[62:63], v[4:5], v[62:63]
	v_pk_mul_f32 v[82:83], v[0:1], v[82:83]
	v_pk_mul_f32 v[84:85], v[8:9], v[62:63]
	s_nop 0
	v_pk_fma_f32 v[84:85], v[12:13], v[82:83], v[84:85] neg_lo:[0,0,1] neg_hi:[0,0,1]
	v_pk_mul_f32 v[12:13], v[12:13], v[62:63]
	s_nop 0
	v_pk_fma_f32 v[8:9], v[8:9], v[82:83], v[12:13]
	v_pk_mul_f32 v[12:13], v[60:61], v[78:79] op_sel_hi:[0,1]
	v_pk_mul_f32 v[60:61], v[60:61], v[80:81] op_sel_hi:[0,1]
	v_pk_mul_f32 v[60:61], v[6:7], v[60:61]
	v_pk_mul_f32 v[12:13], v[2:3], v[12:13]
	v_pk_mul_f32 v[62:63], v[10:11], v[60:61]
	v_cvt_pk_bf16_f32 v8, v8, v9
	v_pk_fma_f32 v[62:63], v[14:15], v[12:13], v[62:63] neg_lo:[0,0,1] neg_hi:[0,0,1]
	v_pk_mul_f32 v[14:15], v[14:15], v[60:61]
	s_nop 0
	v_pk_fma_f32 v[10:11], v[10:11], v[12:13], v[14:15]
	v_lshlrev_b32_e32 v14, 16, v76
	v_and_b32_e32 v15, 0xffff0000, v76
	v_pk_mul_f32 v[60:61], v[14:15], v[14:15]
	v_cvt_pk_bf16_f32 v9, v10, v11
	v_add_f32_e32 v13, v60, v61
	v_cvt_pk_bf16_f32 v12, v84, v85
	s_nop 0
	v_add_f32_dpp v13, v13, v13 quad_perm:[1,0,3,2] row_mask:0xf bank_mask:0xf bound_ctrl:1
	s_nop 1
	v_add_f32_dpp v13, v13, v13 quad_perm:[2,3,0,1] row_mask:0xf bank_mask:0xf bound_ctrl:1
	s_nop 1
	v_add_f32_dpp v13, v13, v13 row_half_mirror row_mask:0xf bank_mask:0xf bound_ctrl:1
	s_nop 1
	v_add_f32_dpp v13, v13, v13 row_mirror row_mask:0xf bank_mask:0xf bound_ctrl:1
	v_mov_b32_e32 v60, v13
	s_nop 1
	v_permlane16_swap_b32_e32 v13, v60
	v_add_f32_e32 v13, v13, v60
	v_fmamk_f32 v13, v13, 0x3c800000, v240
	v_rsq_f32_e32 v60, v13
	v_cvt_pk_bf16_f32 v13, v62, v63
	v_pk_mul_f32 v[10:11], v[60:61], v[14:15] op_sel_hi:[0,1]
	v_pk_mul_f32 v[10:11], v[28:29], v[10:11]
	v_lshlrev_b32_e32 v60, 16, v70
	v_and_b32_e32 v61, 0xffff0000, v70
	v_mov_b32_dpp v14, v10 row_ror:8 row_mask:0xf bank_mask:0xf bound_ctrl:1
	v_mov_b32_dpp v15, v11 row_ror:8 row_mask:0xf bank_mask:0xf bound_ctrl:1
	v_pk_mul_f32 v[14:15], v[50:51], v[14:15]
	v_lshlrev_b32_e32 v50, 16, v73
	v_and_b32_e32 v51, 0xffff0000, v73
	v_pk_mul_f32 v[76:77], v[50:51], v[50:51]
	v_pk_mul_f32 v[62:63], v[60:61], v[60:61]
	v_add_f32_e32 v70, v76, v77
	v_add_f32_e32 v62, v70, v62
	v_add_f32_e32 v62, v63, v62
	v_cndmask_b32_e64 v15, v15, -v15, s[42:43]
	v_cndmask_b32_e64 v14, v14, -v14, s[42:43]
	v_add_f32_dpp v62, v62, v62 quad_perm:[1,0,3,2] row_mask:0xf bank_mask:0xf bound_ctrl:1
	v_pk_fma_f32 v[10:11], v[44:45], v[10:11], v[14:15]
	s_nop 0
	s_nop 0
	v_add_f32_dpp v62, v62, v62 quad_perm:[2,3,0,1] row_mask:0xf bank_mask:0xf bound_ctrl:1
	s_nop 0
	s_nop 0
	s_nop 0
	s_nop 0
	v_add_f32_dpp v62, v62, v62 row_half_mirror row_mask:0xf bank_mask:0xf bound_ctrl:1
	s_nop 1
	v_add_f32_dpp v62, v62, v62 row_mirror row_mask:0xf bank_mask:0xf bound_ctrl:1
	v_mov_b32_e32 v63, v62
	s_nop 1
	v_permlane16_swap_b32_e32 v62, v63
	v_add_f32_e32 v62, v62, v63
	v_mov_b32_e32 v63, v62
	s_nop 1
	v_permlane32_swap_b32_e32 v62, v63
	v_add_f32_e32 v62, v62, v63
	v_fmamk_f32 v62, v62, 0x3b800000, v240
	v_rsq_f32_e32 v62, v62
	v_cvt_pk_bf16_f32 v63, v10, v11
	v_pk_mul_f32 v[10:11], v[62:63], v[50:51] op_sel_hi:[0,1]
	v_pk_mul_f32 v[10:11], v[30:31], v[10:11]
	v_pk_mul_f32 v[44:45], v[62:63], v[60:61] op_sel_hi:[0,1]
	v_cvt_pk_bf16_f32 v50, v10, v11
	v_lshlrev_b32_e32 v10, 16, v69
	v_and_b32_e32 v11, 0xffff0000, v69
	v_pk_mul_f32 v[14:15], v[10:11], v[10:11]
	v_pk_mul_f32 v[44:45], v[32:33], v[44:45]
	v_add_f32_e32 v14, v14, v15
	s_nop 0
	s_nop 0
	v_add_f32_dpp v14, v14, v14 quad_perm:[1,0,3,2] row_mask:0xf bank_mask:0xf bound_ctrl:1
	s_nop 1
	v_add_f32_dpp v14, v14, v14 quad_perm:[2,3,0,1] row_mask:0xf bank_mask:0xf bound_ctrl:1
	s_nop 1
	v_add_f32_dpp v14, v14, v14 row_half_mirror row_mask:0xf bank_mask:0xf bound_ctrl:1
	s_nop 1
	v_add_f32_dpp v14, v14, v14 row_mirror row_mask:0xf bank_mask:0xf bound_ctrl:1
	v_mov_b32_e32 v15, v14
	s_nop 1
	v_permlane16_swap_b32_e32 v14, v15
	v_add_f32_e32 v14, v14, v15
	v_mov_b32_e32 v15, v14
	s_nop 1
	v_permlane32_swap_b32_e32 v14, v15
	v_add_f32_e32 v14, v14, v15
	v_fmamk_f32 v14, v14, 0x3c000000, v240
	v_rsq_f32_e32 v14, v14
	v_cvt_pk_bf16_f32 v15, v44, v45
	s_nop 0
	s_nop 0
	v_pk_mul_f32 v[10:11], v[14:15], v[10:11] op_sel_hi:[0,1]
	s_nop 0
	v_pk_mul_f32 v[10:11], v[40:41], v[10:11]
	s_nop 0
	v_cvt_pk_bf16_f32 v14, v10, v11
	v_add_co_u32_e32 v10, vcc, s22, v66
	s_mov_b32 s22, 0x6401000
	s_nop 0
	v_addc_co_u32_e32 v11, vcc, 0, v67, vcc
	s_cmpk_gt_i32 s11, 0x6fff
	s_cbranch_scc1 .Lt1_wa
	s_waitcnt vmcnt(20)
	s_branch .Lt1_wd
.Lt1_wa:
	s_cmpk_gt_i32 s11, 0x77ff
	s_cbranch_scc1 .Lt1_w0
	s_waitcnt vmcnt(10)
	s_branch .Lt1_wd

.Lt1_wd:
	global_store_dwordx2 v[10:11], v[12:13], off offset:1024
	global_store_dwordx2 v[10:11], v[8:9], off offset:1088
	v_add_co_u32_e32 v8, vcc, s22, v64
	s_mov_b64 s[22:23], 0xd00000
	s_nop 0
	v_addc_co_u32_e32 v9, vcc, 0, v65, vcc
	global_store_dword v[8:9], v63, off offset:1024
	v_lshl_add_u64 v[8:9], s[18:19], 0, v[42:43]
	v_add_co_u32_e32 v8, vcc, 0x1d400000, v8
	v_lshl_add_u64 v[42:43], v[42:43], 0, s[4:5]
	s_nop 0
	v_addc_co_u32_e32 v9, vcc, 0, v9, vcc
	global_store_dword v[8:9], v50, off
	global_store_dword v[8:9], v15, off offset:256
	global_store_dword v[8:9], v14, off offset:512
	global_store_dword v[8:9], v161, off offset:768
	v_lshl_add_u64 v[46:47], v[46:47], 0, s[22:23]
	v_lshl_add_u64 v[48:49], v[48:49], 0, s[22:23]
	s_cmp_eq_u32 s99, 0
	s_cbranch_scc1 .Lt1_c0
	s_cmp_eq_u32 s99, 1
	s_cbranch_scc1 .Lt1_c1
	v_mov_b32_e32 v73, v71
	v_mov_b32_e32 v70, v72
	v_mov_b32_e32 v76, v75
	v_mov_b32_e32 v69, v74
	v_mov_b64_e32 v[60:61], v[56:57]
	v_mov_b64_e32 v[44:45], v[52:53]
	v_mov_b64_e32 v[12:13], v[16:17]
	v_mov_b64_e32 v[8:9], v[20:21]
	v_mov_b64_e32 v[62:63], v[58:59]
	v_mov_b64_e32 v[14:15], v[18:19]
	v_mov_b64_e32 v[10:11], v[22:23]
	v_mov_b64_e32 v[50:51], v[54:55]
	s_mov_b32 s99, 0
	s_branch .Lt1_latch
.Lt1_c0:
	v_mov_b32_e32 v73, v112
	v_mov_b32_e32 v70, v113
	v_mov_b32_e32 v76, v115
	v_mov_b32_e32 v69, v114
	v_mov_b64_e32 v[60:61], v[108:109]
	v_mov_b64_e32 v[44:45], v[104:105]
	v_mov_b64_e32 v[12:13], v[96:97]
	v_mov_b64_e32 v[8:9], v[100:101]
	v_mov_b64_e32 v[62:63], v[110:111]
	v_mov_b64_e32 v[14:15], v[98:99]
	v_mov_b64_e32 v[10:11], v[102:103]
	v_mov_b64_e32 v[50:51], v[106:107]
	s_mov_b32 s99, 1
	s_branch .Lt1_latch
.Lt1_c1:
	v_mov_b32_e32 v73, v132
	v_mov_b32_e32 v70, v133
	v_mov_b32_e32 v76, v135
	v_mov_b32_e32 v69, v134
	v_mov_b64_e32 v[60:61], v[128:129]
	v_mov_b64_e32 v[44:45], v[124:125]
	v_mov_b64_e32 v[12:13], v[116:117]
	v_mov_b64_e32 v[8:9], v[120:121]
	v_mov_b64_e32 v[62:63], v[130:131]
	v_mov_b64_e32 v[14:15], v[118:119]
	v_mov_b64_e32 v[10:11], v[122:123]
	v_mov_b64_e32 v[50:51], v[126:127]
	s_mov_b32 s99, 2

.LBB0_270:
	s_cmpk_gt_i32 s11, 0x77ff
	s_cselect_b64 s[2:3], -1, 0
	v_lshl_add_u64 v[66:67], s[18:19], 0, v[46:47]
	v_lshl_add_u64 v[64:65], s[18:19], 0, v[48:49]
	s_cmpk_gt_i32 s11, 0x67ff
	s_cbranch_scc1 .LBB0_269
	s_cmp_eq_u32 s99, 0
	s_cbranch_scc1 .Lt1_i0
	s_cmp_eq_u32 s99, 1
	s_cbranch_scc1 .Lt1_i1
	s_and_b32 s22, s10, 0xffe0
	s_lshr_b32 s31, s11, 2
	v_add_co_u32_e32 v116, vcc, 0x8b00000, v66
	s_lshl_b32 s96, s22, 2
	s_and_b32 s22, s7, 0x3f0
	s_and_b32 s31, s31, 0x1f0
	v_addc_co_u32_e32 v117, vcc, 0, v67, vcc
	s_or_b32 s23, s22, 0x70400
	s_or_b32 s33, s31, 0x70000
	v_add_co_u32_e32 v118, vcc, 0x8b00000, v64
	v_mov_b32_e32 v122, s33
	v_mov_b32_e32 v123, s23
	s_or_b32 s22, s22, 0x70800
	s_or_b32 s23, s31, 0x70200
	v_addc_co_u32_e32 v119, vcc, 0, v65, vcc
	v_cndmask_b32_e64 v122, v122, v123, s[40:41]
	v_mov_b32_e32 v126, s23
	v_mov_b32_e32 v127, s22
	global_load_dwordx2 v[130:131], v[116:117], off offset:1024
	global_load_dwordx2 v[128:129], v[116:117], off offset:1088
	global_load_dword v132, v[118:119], off offset:3072
	global_load_dword v133, v[118:119], off offset:3328
	v_add_co_u32_e32 v116, vcc, 0x8b01000, v64
	v_lshlrev_b32_e32 v160, 2, v122
	v_cndmask_b32_e64 v126, v126, v127, s[40:41]
	v_addc_co_u32_e32 v117, vcc, 0, v65, vcc
	v_lshl_add_u64 v[120:121], v[34:35], 0, s[96:97]
	v_lshl_add_u64 v[124:125], v[38:39], 0, v[160:161]
	v_lshlrev_b32_e32 v160, 2, v126
	global_load_dword v134, v[118:119], off offset:3584
	global_load_dword v135, v[116:117], off offset:1024
	s_nop 0
	global_load_dwordx4 v[116:119], v[120:121], off
	v_lshl_add_u64 v[120:121], v[36:37], 0, s[96:97]
	v_lshl_add_u64 v[126:127], v[38:39], 0, v[160:161]
	global_load_dwordx4 v[120:123], v[120:121], off
	s_nop 0
	global_load_dwordx2 v[124:125], v[124:125], off
	s_nop 0
	global_load_dwordx2 v[126:127], v[126:127], off
	s_branch .LBB0_269
.Lt1_i0:
	s_and_b32 s22, s10, 0xffe0
	s_lshr_b32 s31, s11, 2
	v_add_co_u32_e32 v16, vcc, 0x8b00000, v66
	s_lshl_b32 s96, s22, 2
	s_and_b32 s22, s7, 0x3f0
	s_and_b32 s31, s31, 0x1f0
	v_addc_co_u32_e32 v17, vcc, 0, v67, vcc
	s_or_b32 s23, s22, 0x70400
	s_or_b32 s33, s31, 0x70000
	v_add_co_u32_e32 v18, vcc, 0x8b00000, v64
	v_mov_b32_e32 v22, s33
	v_mov_b32_e32 v23, s23
	s_or_b32 s22, s22, 0x70800
	s_or_b32 s23, s31, 0x70200
	v_addc_co_u32_e32 v19, vcc, 0, v65, vcc
	v_cndmask_b32_e64 v22, v22, v23, s[40:41]
	v_mov_b32_e32 v54, s23
	v_mov_b32_e32 v55, s22
	global_load_dwordx2 v[58:59], v[16:17], off offset:1024
	global_load_dwordx2 v[56:57], v[16:17], off offset:1088
	global_load_dword v71, v[18:19], off offset:3072
	global_load_dword v72, v[18:19], off offset:3328
	v_add_co_u32_e32 v16, vcc, 0x8b01000, v64
	v_lshlrev_b32_e32 v160, 2, v22
	v_cndmask_b32_e64 v54, v54, v55, s[40:41]
	v_addc_co_u32_e32 v17, vcc, 0, v65, vcc
	v_lshl_add_u64 v[20:21], v[34:35], 0, s[96:97]
	v_lshl_add_u64 v[52:53], v[38:39], 0, v[160:161]
	v_lshlrev_b32_e32 v160, 2, v54
	global_load_dword v74, v[18:19], off offset:3584
	global_load_dword v75, v[16:17], off offset:1024
	s_nop 0
	global_load_dwordx4 v[16:19], v[20:21], off
	v_lshl_add_u64 v[20:21], v[36:37], 0, s[96:97]
	v_lshl_add_u64 v[54:55], v[38:39], 0, v[160:161]
	global_load_dwordx4 v[20:23], v[20:21], off
	s_nop 0
	global_load_dwordx2 v[52:53], v[52:53], off
	s_nop 0
	global_load_dwordx2 v[54:55], v[54:55], off
	s_branch .LBB0_269
.Lt1_i1:
	s_and_b32 s22, s10, 0xffe0
	s_lshr_b32 s31, s11, 2
	v_add_co_u32_e32 v96, vcc, 0x8b00000, v66
	s_lshl_b32 s96, s22, 2
	s_and_b32 s22, s7, 0x3f0
	s_and_b32 s31, s31, 0x1f0
	v_addc_co_u32_e32 v97, vcc, 0, v67, vcc
	s_or_b32 s23, s22, 0x70400
	s_or_b32 s33, s31, 0x70000
	v_add_co_u32_e32 v98, vcc, 0x8b00000, v64
	v_mov_b32_e32 v102, s33
	v_mov_b32_e32 v103, s23
	s_or_b32 s22, s22, 0x70800
	s_or_b32 s23, s31, 0x70200
	v_addc_co_u32_e32 v99, vcc, 0, v65, vcc
	v_cndmask_b32_e64 v102, v102, v103, s[40:41]
	v_mov_b32_e32 v106, s23
	v_mov_b32_e32 v107, s22
	global_load_dwordx2 v[110:111], v[96:97], off offset:1024
	global_load_dwordx2 v[108:109], v[96:97], off offset:1088
	global_load_dword v112, v[98:99], off offset:3072
	global_load_dword v113, v[98:99], off offset:3328
	v_add_co_u32_e32 v96, vcc, 0x8b01000, v64
	v_lshlrev_b32_e32 v160, 2, v102
	v_cndmask_b32_e64 v106, v106, v107, s[40:41]
	v_addc_co_u32_e32 v97, vcc, 0, v65, vcc
	v_lshl_add_u64 v[100:101], v[34:35], 0, s[96:97]
	v_lshl_add_u64 v[104:105], v[38:39], 0, v[160:161]
	v_lshlrev_b32_e32 v160, 2, v106
	global_load_dword v114, v[98:99], off offset:3584
	global_load_dword v115, v[96:97], off offset:1024
	s_nop 0
	global_load_dwordx4 v[96:99], v[100:101], off
	v_lshl_add_u64 v[100:101], v[36:37], 0, s[96:97]
	v_lshl_add_u64 v[106:107], v[38:39], 0, v[160:161]
	global_load_dwordx4 v[100:103], v[100:101], off
	s_nop 0
	global_load_dwordx2 v[104:105], v[104:105], off
	s_nop 0
	global_load_dwordx2 v[106:107], v[106:107], off
	s_branch .LBB0_269
